# combo12 + strategy 7.5: 107 packed VOP3P fp32 ops (fma/add/mul by a broadcast scalar) in the attention softmax chains split into single ops
# baseline (speedup 1.0000x reference)
.LBB0_497:
	v_mul_hi_i32 v1, v2, s84
	v_lshrrev_b32_e32 v9, 31, v1
	v_ashrrev_i32_e32 v1, 7, v1
	v_add_u32_e32 v1, v1, v9
	v_mul_hi_i32 v9, v3, s84
	v_lshrrev_b32_e32 v10, 31, v9
	v_ashrrev_i32_e32 v9, 7, v9
	v_add_u32_e32 v9, v9, v10
	v_mul_lo_u32 v10, v9, s85
	v_mul_lo_u32 v11, v1, s85
	v_sub_u32_e32 v11, v2, v11
	v_sub_u32_e32 v10, v3, v10
	v_add_u32_e32 v1, s0, v1
	v_max_i32_e32 v12, 0x200, v10
	v_max_i32_e32 v10, 0x200, v11
	v_add_u32_e32 v9, s0, v9
	v_lshl_add_u32 v1, v1, 8, v1
	v_lshl_add_u32 v9, v9, 8, v9
	v_add3_u32 v10, v10, v1, s96
	v_add3_u32 v12, v12, v9, s96
	v_ashrrev_i32_e32 v11, 31, v10
	v_ashrrev_i32_e32 v13, 31, v12
	s_waitcnt lgkmcnt(0)
	v_lshl_add_u64 v[10:11], v[10:11], 2, s[4:5]
	v_lshl_add_u64 v[12:13], v[12:13], 2, s[4:5]
	global_load_dword v10, v[10:11], off offset:512
	s_nop 0
	global_load_dword v11, v[12:13], off offset:512
	v_add_u32_e32 v9, 0x400, v2
	v_add_u32_e32 v1, 0x400, v3
	v_add_u32_e32 v7, -2, v7
	s_add_i32 s1, s1, 4
	v_cmp_eq_u32_e32 vcc, 0, v7
	v_add_u32_e32 v3, 0x800, v3
	v_add_u32_e32 v2, 0x800, v2
	s_or_b64 s[10:11], vcc, s[10:11]
	s_waitcnt vmcnt(0)
	v_mul_f32_e32 v10, s64, v10
	v_mul_f32_e32 v11, s64, v11
	ds_write2st64_b32 v8, v10, v11 offset1:8
	v_mul_hi_i32 v10, v9, s84
	v_lshrrev_b32_e32 v11, 31, v10
	v_ashrrev_i32_e32 v10, 7, v10
	v_add_u32_e32 v10, v10, v11
	v_mul_hi_i32 v11, v1, s84
	v_lshrrev_b32_e32 v12, 31, v11
	v_ashrrev_i32_e32 v11, 7, v11
	v_add_u32_e32 v11, v11, v12
	v_mul_lo_u32 v13, v10, s85
	v_mul_lo_u32 v12, v11, s85
	v_sub_u32_e32 v9, v9, v13
	v_add_u32_e32 v10, s0, v10
	v_sub_u32_e32 v1, v1, v12
	v_max_i32_e32 v9, 0x200, v9
	v_add_u32_e32 v11, s0, v11
	v_lshl_add_u32 v10, v10, 8, v10
	v_max_i32_e32 v1, 0x200, v1
	v_lshl_add_u32 v11, v11, 8, v11
	v_add3_u32 v10, v9, v10, s96
	v_add3_u32 v12, v1, v11, s96
	v_ashrrev_i32_e32 v11, 31, v10
	v_ashrrev_i32_e32 v13, 31, v12
	v_lshl_add_u64 v[10:11], v[10:11], 2, s[4:5]
	v_lshl_add_u64 v[12:13], v[12:13], 2, s[4:5]
	global_load_dword v10, v[10:11], off offset:512
	s_nop 0
	global_load_dword v11, v[12:13], off offset:512
	v_mov_b32_e32 v1, s1
	s_waitcnt vmcnt(0)
	v_mul_f32_e32 v10, s64, v10
	v_mul_f32_e32 v11, s64, v11
	ds_write2st64_b32 v8, v10, v11 offset0:16 offset1:24
	v_add_u32_e32 v8, 0x2000, v8
	s_andn2_b64 exec, exec, s[10:11]
	s_cbranch_execnz .LBB0_497
	s_or_b64 exec, exec, s[10:11]
	v_lshlrev_b32_e32 v7, 9, v1
.LBB0_499:
	s_or_b64 exec, exec, s[8:9]
	v_and_b32_e32 v1, 2, v6
	v_cmp_eq_u32_e32 vcc, 0, v1
	s_and_saveexec_b64 s[8:9], vcc
	s_cbranch_execz .LBB0_501
	v_mul_hi_i32 v1, v2, s84
	v_lshrrev_b32_e32 v6, 31, v1
	v_ashrrev_i32_e32 v1, 7, v1
	v_add_u32_e32 v1, v1, v6
	v_mul_hi_i32 v6, v3, s84
	v_lshrrev_b32_e32 v8, 31, v6
	v_ashrrev_i32_e32 v6, 7, v6
	v_add_u32_e32 v6, v6, v8
	v_mul_lo_u32 v9, v1, s85
	v_mul_lo_u32 v8, v6, s85
	v_sub_u32_e32 v2, v2, v9
	v_add_u32_e32 v1, s0, v1
	v_sub_u32_e32 v3, v3, v8
	v_max_i32_e32 v2, 0x200, v2
	v_add_u32_e32 v6, s0, v6
	v_lshl_add_u32 v1, v1, 8, v1
	v_max_i32_e32 v3, 0x200, v3
	v_lshl_add_u32 v6, v6, 8, v6
	v_add3_u32 v2, v2, v1, s96
	v_add3_u32 v8, v3, v6, s96
	v_ashrrev_i32_e32 v3, 31, v2
	v_ashrrev_i32_e32 v9, 31, v8
	s_waitcnt lgkmcnt(0)
	v_lshl_add_u64 v[2:3], v[2:3], 2, s[4:5]
	v_lshl_add_u64 v[8:9], v[8:9], 2, s[4:5]
	global_load_dword v2, v[2:3], off offset:512
	s_nop 0
	global_load_dword v3, v[8:9], off offset:512
	v_add_u32_e32 v1, v0, v7
	v_lshl_add_u32 v1, v1, 2, 0
	s_waitcnt vmcnt(0)
	v_mul_f32_e32 v2, s64, v2
	v_mul_f32_e32 v3, s64, v3
	ds_write2st64_b32 v1, v2, v3 offset0:192 offset1:200

.LBB0_513:
	v_readlane_b32 s4, v255, 2
	v_mov_b32_e32 v8, s0
	v_readlane_b32 s0, v255, 4
	v_mov_b32_e32 v7, s10
	v_readlane_b32 s5, v255, 3
	v_readlane_b32 s1, v255, 5
	s_bfe_u32 s72, s54, 0x20001
	v_cndmask_b32_e64 v7, 0, v7, s[4:5]
	v_cndmask_b32_e64 v8, 0, v8, s[0:1]
	v_readlane_b32 s0, v255, 6
	v_add_f32_e32 v7, v7, v8
	v_mov_b32_e32 v8, s11
	v_readlane_b32 s1, v255, 7
	s_mov_b32 s4, s61
	s_mov_b64 s[10:11], -1
	v_cndmask_b32_e64 v8, 0, v8, s[0:1]
	v_add_f32_e32 v7, v8, v7
	v_add_f32_e32 v5, v5, v7
	v_sub_f32_e32 v4, v5, v4
	v_add_f32_e32 v4, v4, v6
	v_add_f32_e32 v0, v0, v4
	v_add_f32_e32 v1, v1, v0
	v_add_f32_e32 v2, v2, v1
	v_add_f32_e32 v3, v3, v2
	s_mov_b32 s0, 0xbfb8aa3b
	v_mul_f32_e32 v0, s0, v0
	v_mul_f32_e32 v1, s0, v1
	v_mul_f32_e32 v2, s0, v2
	v_mul_f32_e32 v3, s0, v3
	s_and_b32 s1, s54, 3
	s_cmp_eq_u32 s1, 1
	s_cselect_b32 s0, 5, 1
	s_ashr_i32 s36, s54, 3
	ds_write_b128 v186, v[0:3] offset:32768
	s_waitcnt lgkmcnt(0)
	s_barrier
	v_mbcnt_lo_u32_b32 v0, -1, 0
	v_mbcnt_hi_u32_b32 v0, -1, v0
	s_and_b32 s0, s0, s54
	s_mul_i32 s5, s36, 0xc00000
	v_lshl_or_b32 v2, s4, 6, v0
	s_mul_hi_i32 s4, s36, 0xc00000
	s_add_u32 s84, s51, s5
	s_addc_u32 s85, s64, s4
	v_and_b32_e32 v1, 15, v0
	s_cmp_lt_i32 s1, 2
	s_cbranch_scc1 .LBB0_519
	s_cmp_gt_i32 s1, 2
	s_cbranch_scc0 .LBB0_516
	v_readfirstlane_b32 s6, v2
	s_lshr_b32 s6, s6, 1
	s_lshl_b32 s7, s0, 8
	s_and_b32 s6, s6, 0x1fffe0
	s_add_i32 s6, s6, s7
	v_or_b32_e32 v3, s6, v1
	s_lshl_b32 s6, s72, 7
	v_and_b32_e32 v4, 48, v0
	v_mul_u32_u24_e32 v3, 0x1800, v3
	s_add_u32 s8, s84, s6
	v_or3_b32 v3, s6, v4, v3
	s_addc_u32 s9, s85, 0
	s_lshl_b32 s6, s36, 2
	s_or_b32 s6, s6, s72
	s_addk_i32 s6, 0x100
	s_ashr_i32 s7, s6, 31
	s_lshl_b64 s[6:7], s[6:7], 18
	s_add_u32 s10, s2, s6
	s_addc_u32 s11, s3, s7
	s_lshl_b32 s6, s0, 2
	v_add_u32_e32 v4, 0xc00, v3
	v_add_u32_e32 v3, 0x18c00, v3
	s_add_i32 s6, s6, -8
	global_load_dwordx4 v[24:27], v4, s[84:85]
	global_load_dwordx4 v[28:31], v4, s[84:85] offset:64
	global_load_dwordx4 v[32:35], v3, s[84:85]
	global_load_dwordx4 v[36:39], v3, s[84:85] offset:64
	v_ashrrev_i32_e32 v3, 3, v2
	s_cmp_gt_u32 s0, 1
	v_lshrrev_b32_e32 v6, 2, v3
	s_cselect_b32 s12, s6, 0
	v_and_b32_e32 v4, 7, v0
	v_and_b32_e32 v6, 6, v6
	v_bfe_u32 v8, v3, 1, 1
	s_lshl_b32 s6, s12, 6
	s_mul_i32 s7, s12, 0x60000
	v_mul_lo_u32 v5, v3, s71
	v_bitop3_b32 v4, v6, v4, v8 bitop3:0x36
	s_mul_hi_u32 s13, s6, 0x1800
	s_add_u32 s6, s8, s7
	v_lshrrev_b32_e32 v7, 1, v3
	v_lshl_or_b32 v4, v4, 4, v5
	s_addc_u32 s7, s9, s13
	v_xor_b32_e32 v5, v7, v0
	global_load_dwordx4 v[8:11], v4, s[6:7] offset:3584
	s_lshl_b32 s6, s12, 7
	v_lshlrev_b32_e32 v3, 12, v3
	v_lshlrev_b32_e32 v5, 4, v5
	s_add_u32 s6, s10, s6
	v_and_or_b32 v3, v5, s97, v3
	s_addc_u32 s7, s11, 0
	s_or_b32 s12, s12, 1
	global_load_dwordx4 v[12:15], v3, s[6:7]
	s_lshl_b32 s6, s12, 6
	s_mul_i32 s7, s12, 0x60000
	s_mul_hi_u32 s13, s6, 0x1800
	s_add_u32 s6, s8, s7
	s_addc_u32 s7, s9, s13
	global_load_dwordx4 v[16:19], v4, s[6:7] offset:3584
	s_lshl_b32 s6, s12, 7
	s_add_u32 s6, s10, s6
	s_addc_u32 s7, s11, 0
	global_load_dwordx4 v[20:23], v3, s[6:7]
	s_mov_b64 s[10:11], 0

.LBB0_550:
	s_lshl_b32 s5, s23, 13
	s_add_i32 s4, s29, 0xffffff80
	s_cmp_lt_i32 s4, s26
	s_cselect_b64 s[6:7], -1, 0
	s_cmp_gt_i32 s4, s25
	s_cselect_b64 s[8:9], -1, 0
	v_add_u32_e32 v0, s5, v235
	s_or_b64 s[6:7], s[6:7], s[8:9]
	v_add_u32_e32 v215, s5, v236
	s_and_b64 vcc, exec, s[6:7]
	v_add_u32_e32 v245, v0, v232
	v_add_u32_e32 v244, v0, v231
	s_cbranch_vccnz .LBB0_554
	ds_read_b128 v[140:143], v245
	ds_read_b128 v[144:147], v245 offset:512
	ds_read_b128 v[148:151], v244
	ds_read_b128 v[152:155], v244 offset:512
	v_add_u32_e32 v136, v215, v232
	ds_read_b128 v[124:127], v136 offset:16384
	ds_read_b128 v[128:131], v136 offset:18432
	s_waitcnt lgkmcnt(5)
	v_mfma_f32_16x16x32_bf16 v[0:3], v[140:143], v[24:27], 0
	ds_read_b128 v[132:135], v136 offset:20480
	ds_read_b128 v[136:139], v136 offset:22528
	s_add_i32 s5, s29, 31
	s_cmp_le_i32 s5, s22
	s_waitcnt lgkmcnt(6)
	v_mfma_f32_16x16x32_bf16 v[4:7], v[144:147], v[24:27], 0
	s_cselect_b64 s[18:19], -1, 0
	s_mov_b64 s[20:21], -1
	s_and_b64 vcc, exec, s[18:19]
	s_waitcnt lgkmcnt(5)
	v_mfma_f32_16x16x32_bf16 v[156:159], v[148:151], v[28:31], v[0:3]
	s_waitcnt lgkmcnt(4)
	v_mfma_f32_16x16x32_bf16 v[160:163], v[152:155], v[28:31], v[4:7]
	s_cbranch_vccz .LBB0_557
	s_add_i32 s5, s27, 0
	v_mov_b32_e32 v0, s5
	ds_read_b32 v0, v0 offset:49152
	v_cmp_eq_f32_e32 vcc, v242, v233
	s_waitcnt lgkmcnt(0)
	v_sub_f32_e32 v6, v208, v0
	v_fma_f32 v0, v156, s58, -v6
	v_fma_f32 v1, v157, s58, -v6
	v_fma_f32 v2, v158, s58, -v6
	v_fma_f32 v3, v159, s58, -v6
	v_fma_f32 v4, v160, s58, -v6
	v_fma_f32 v5, v161, s58, -v6
	v_fma_f32 v210, v162, s58, -v6
	v_fma_f32 v211, v163, s58, -v6
	v_max3_f32 v6, v0, v1, v2
	v_max3_f32 v7, v3, v4, v5
	s_nop 0
	v_max3_f32 v164, v210, v211, v211
	s_nop 0
	v_max3_f32 v6, v6, v7, v164
	v_cndmask_b32_e32 v7, v226, v233, vcc
	v_cmp_gt_f32_e32 vcc, v6, v7
	s_cbranch_vccz .LBB0_555
	v_add_f32_e32 v6, v208, v6
	v_mov_b32_e32 v7, v6
	s_nop 1
	v_permlane16_swap_b32 v6, v7
	s_nop 0
	v_max_f32_e32 v7, v7, v7
	v_max_f32_e32 v6, v6, v6
	v_max_f32_e32 v6, v6, v7
	v_mov_b32_e32 v7, v6
	s_nop 1
	v_permlane32_swap_b32 v6, v7
	s_nop 0
	v_max3_f32 v243, v242, v6, v7
	v_cmp_neq_f32_e32 vcc, v243, v233
	s_nop 1
	v_cndmask_b32_e32 v212, 0, v243, vcc
	v_sub_f32_e32 v6, v242, v212
	v_exp_f32_e32 v6, v6
	v_sub_f32_e32 v7, v212, v208
	v_sub_f32_e32 v0, v0, v7
	v_sub_f32_e32 v1, v1, v7
	v_pk_mul_f32 v[110:111], v[110:111], v[6:7] op_sel_hi:[1,0]
	v_pk_mul_f32 v[108:109], v[108:109], v[6:7] op_sel_hi:[1,0]
	v_pk_mul_f32 v[102:103], v[102:103], v[6:7] op_sel_hi:[1,0]
	v_pk_mul_f32 v[100:101], v[100:101], v[6:7] op_sel_hi:[1,0]
	v_pk_mul_f32 v[98:99], v[98:99], v[6:7] op_sel_hi:[1,0]
	v_pk_mul_f32 v[96:97], v[96:97], v[6:7] op_sel_hi:[1,0]
	v_pk_mul_f32 v[94:95], v[94:95], v[6:7] op_sel_hi:[1,0]
	v_pk_mul_f32 v[92:93], v[92:93], v[6:7] op_sel_hi:[1,0]
	v_pk_mul_f32 v[90:91], v[90:91], v[6:7] op_sel_hi:[1,0]
	v_pk_mul_f32 v[88:89], v[88:89], v[6:7] op_sel_hi:[1,0]
	v_sub_f32_e32 v2, v2, v7
	v_sub_f32_e32 v3, v3, v7
	v_sub_f32_e32 v4, v4, v7
	v_sub_f32_e32 v5, v5, v7
	v_sub_f32_e32 v210, v210, v7
	v_sub_f32_e32 v211, v211, v7
	s_branch .LBB0_556

.LBB0_557:
	s_and_b64 vcc, exec, s[20:21]
	s_cbranch_vccz .LBB0_561
	ds_read2_b32 v[0:1], v239 offset0:16 offset1:17
	ds_read2_b32 v[2:3], v239 offset0:18 offset1:19
	ds_read2_b32 v[4:5], v239 offset0:20 offset1:21
	ds_read2_b32 v[6:7], v239 offset0:22 offset1:23
	s_waitcnt lgkmcnt(3)
	v_fma_f32 v0, v156, s58, v0
	v_fma_f32 v1, v157, s58, v1
	s_waitcnt lgkmcnt(2)
	v_fma_f32 v2, v158, s58, v2
	v_fma_f32 v3, v159, s58, v3
	s_waitcnt lgkmcnt(1)
	v_fma_f32 v4, v160, s58, v4
	v_fma_f32 v5, v161, s58, v5
	v_max3_f32 v156, v0, v1, v2
	s_waitcnt lgkmcnt(0)
	v_fma_f32 v6, v162, s58, v6
	v_fma_f32 v7, v163, s58, v7
	v_max3_f32 v157, v3, v4, v5
	s_nop 0
	v_max3_f32 v158, v6, v7, v7
	s_nop 0
	v_max3_f32 v156, v156, v157, v158
	v_add_f32_e32 v157, 0x41800000, v242
	v_cmp_gt_f32_e32 vcc, v156, v157
	s_cbranch_vccz .LBB0_560
	v_mov_b32_e32 v157, v156
	s_nop 1
	v_permlane16_swap_b32 v157, v156
	s_nop 0
	v_max_f32_e32 v156, v156, v156
	v_max_f32_e32 v157, v157, v157
	v_max_f32_e32 v156, v157, v156
	v_mov_b32_e32 v157, v156
	s_nop 1
	v_permlane32_swap_b32 v157, v156
	s_nop 0
	v_max3_f32 v157, v242, v157, v156
	v_cmp_neq_f32_e32 vcc, v157, v233
	s_nop 1
	v_cndmask_b32_e32 v208, 0, v157, vcc
	v_sub_f32_e32 v156, v242, v208
	v_exp_f32_e32 v156, v156
	v_mov_b32_e32 v242, v157
	v_pk_mul_f32 v[110:111], v[110:111], v[156:157] op_sel_hi:[1,0]
	v_pk_mul_f32 v[108:109], v[108:109], v[156:157] op_sel_hi:[1,0]
	v_pk_mul_f32 v[102:103], v[102:103], v[156:157] op_sel_hi:[1,0]
	v_pk_mul_f32 v[100:101], v[100:101], v[156:157] op_sel_hi:[1,0]
	v_pk_mul_f32 v[98:99], v[98:99], v[156:157] op_sel_hi:[1,0]
	v_pk_mul_f32 v[96:97], v[96:97], v[156:157] op_sel_hi:[1,0]
	v_pk_mul_f32 v[94:95], v[94:95], v[156:157] op_sel_hi:[1,0]
	v_pk_mul_f32 v[92:93], v[92:93], v[156:157] op_sel_hi:[1,0]
	v_pk_mul_f32 v[90:91], v[90:91], v[156:157] op_sel_hi:[1,0]
	v_pk_mul_f32 v[88:89], v[88:89], v[156:157] op_sel_hi:[1,0]
.LBB0_560:
	v_sub_f32_e32 v0, v0, v208
	v_sub_f32_e32 v1, v1, v208
	v_sub_f32_e32 v2, v2, v208
	v_sub_f32_e32 v3, v3, v208
	v_sub_f32_e32 v4, v4, v208
	v_sub_f32_e32 v5, v5, v208
	v_sub_f32_e32 v210, v6, v208
	v_sub_f32_e32 v211, v7, v208
	v_exp_f32_e32 v0, v0
	v_exp_f32_e32 v1, v1
	v_exp_f32_e32 v2, v2
	v_exp_f32_e32 v3, v3
	v_exp_f32_e32 v4, v4
	v_exp_f32_e32 v5, v5
	v_exp_f32_e32 v6, v210
	v_mov_b32_e32 v212, v208
	v_mov_b32_e32 v243, v242
.LBB0_561:
	v_exp_f32_e32 v7, v211
	v_cvt_pk_bf16_f32 v0, v0, v1
	v_cvt_pk_bf16_f32 v1, v2, v3
	v_cvt_pk_bf16_f32 v2, v4, v5
	v_cvt_pk_bf16_f32 v3, v6, v7
	s_mov_b64 s[20:21], -1
	s_andn2_b64 vcc, exec, s[18:19]
	v_mfma_f32_16x16x32_bf16 v[108:111], v[112:115], v[0:3], v[108:111]
	s_waitcnt lgkmcnt(3)
	v_mfma_f32_16x16x32_bf16 v[100:103], v[124:127], v[0:3], v[100:103]
	s_waitcnt lgkmcnt(2)
	v_mfma_f32_16x16x32_bf16 v[96:99], v[128:131], v[0:3], v[96:99]
	s_waitcnt lgkmcnt(1)
	v_mfma_f32_16x16x32_bf16 v[92:95], v[132:135], v[0:3], v[92:95]
	s_waitcnt lgkmcnt(0)
	v_mfma_f32_16x16x32_bf16 v[88:91], v[136:139], v[0:3], v[88:91]
	v_mfma_f32_16x16x32_bf16 v[0:3], v[140:143], v[32:35], 0
	v_mfma_f32_16x16x32_bf16 v[148:151], v[148:151], v[36:39], v[0:3]
	v_mfma_f32_16x16x32_bf16 v[0:3], v[144:147], v[32:35], 0
	v_mfma_f32_16x16x32_bf16 v[140:143], v[152:155], v[36:39], v[0:3]
	s_cbranch_vccnz .LBB0_566
	s_add_i32 s5, s27, 0
	s_nop 4
	v_mov_b32_e32 v0, s5
	ds_read_b32 v0, v0 offset:49152
	v_cmp_eq_f32_e32 vcc, v214, v233
	s_waitcnt lgkmcnt(0)
	v_sub_f32_e32 v6, v184, v0
	v_fma_f32 v0, v148, s58, -v6
	v_fma_f32 v1, v149, s58, -v6
	v_fma_f32 v2, v150, s58, -v6
	v_fma_f32 v3, v151, s58, -v6
	v_fma_f32 v4, v140, s58, -v6
	v_fma_f32 v5, v141, s58, -v6
	v_fma_f32 v168, v142, s58, -v6
	v_fma_f32 v169, v143, s58, -v6
	v_max3_f32 v6, v0, v1, v2
	v_max3_f32 v7, v3, v4, v5
	s_nop 0
	v_max3_f32 v144, v168, v169, v169
	s_nop 0
	v_max3_f32 v6, v6, v7, v144
	v_cndmask_b32_e32 v7, v226, v233, vcc
	v_cmp_gt_f32_e32 vcc, v6, v7
	s_cbranch_vccz .LBB0_564
	v_add_f32_e32 v6, v184, v6
	v_mov_b32_e32 v7, v6
	s_nop 1
	v_permlane16_swap_b32 v6, v7
	s_nop 0
	v_max_f32_e32 v7, v7, v7
	v_max_f32_e32 v6, v6, v6
	v_max_f32_e32 v6, v6, v7
	v_mov_b32_e32 v7, v6
	s_nop 1
	v_permlane32_swap_b32 v7, v6
	s_nop 0
	v_max3_f32 v211, v214, v7, v6
	v_cmp_neq_f32_e32 vcc, v211, v233
	s_nop 1
	v_cndmask_b32_e32 v210, 0, v211, vcc
	v_sub_f32_e32 v6, v214, v210
	v_exp_f32_e32 v6, v6
	v_sub_f32_e32 v7, v210, v184
	v_sub_f32_e32 v0, v0, v7
	v_sub_f32_e32 v1, v1, v7
	v_pk_mul_f32 v[106:107], v[106:107], v[6:7] op_sel_hi:[1,0]
	v_pk_mul_f32 v[104:105], v[104:105], v[6:7] op_sel_hi:[1,0]
	v_pk_mul_f32 v[86:87], v[86:87], v[6:7] op_sel_hi:[1,0]
	v_pk_mul_f32 v[84:85], v[84:85], v[6:7] op_sel_hi:[1,0]
	v_pk_mul_f32 v[82:83], v[82:83], v[6:7] op_sel_hi:[1,0]
	v_pk_mul_f32 v[80:81], v[80:81], v[6:7] op_sel_hi:[1,0]
	v_pk_mul_f32 v[78:79], v[78:79], v[6:7] op_sel_hi:[1,0]
	v_pk_mul_f32 v[76:77], v[76:77], v[6:7] op_sel_hi:[1,0]
	v_pk_mul_f32 v[74:75], v[74:75], v[6:7] op_sel_hi:[1,0]
	v_pk_mul_f32 v[72:73], v[72:73], v[6:7] op_sel_hi:[1,0]
	v_sub_f32_e32 v2, v2, v7
	v_sub_f32_e32 v3, v3, v7
	v_sub_f32_e32 v4, v4, v7
	v_sub_f32_e32 v5, v5, v7
	v_sub_f32_e32 v168, v168, v7
	v_sub_f32_e32 v169, v169, v7
	s_branch .LBB0_565

.LBB0_566:
	s_and_b64 vcc, exec, s[20:21]
	s_cbranch_vccz .LBB0_570
	s_nop 3
	ds_read2_b32 v[0:1], v239 offset1:1
	ds_read2_b32 v[2:3], v239 offset0:2 offset1:3
	ds_read2_b32 v[4:5], v239 offset0:4 offset1:5
	ds_read2_b32 v[6:7], v239 offset0:6 offset1:7
	s_waitcnt lgkmcnt(3)
	v_fma_f32 v0, v148, s58, v0
	v_fma_f32 v1, v149, s58, v1
	s_waitcnt lgkmcnt(2)
	v_fma_f32 v2, v150, s58, v2
	v_fma_f32 v3, v151, s58, v3
	s_waitcnt lgkmcnt(1)
	v_fma_f32 v4, v140, s58, v4
	v_fma_f32 v5, v141, s58, v5
	v_max3_f32 v140, v0, v1, v2
	s_waitcnt lgkmcnt(0)
	v_fma_f32 v6, v142, s58, v6
	v_fma_f32 v7, v143, s58, v7
	v_max3_f32 v141, v3, v4, v5
	s_nop 0
	v_max3_f32 v142, v6, v7, v7
	s_nop 0
	v_max3_f32 v140, v140, v141, v142
	v_add_f32_e32 v141, 0x41800000, v214
	v_cmp_gt_f32_e32 vcc, v140, v141
	s_cbranch_vccz .LBB0_569
	v_mov_b32_e32 v141, v140
	s_nop 1
	v_permlane16_swap_b32 v141, v140
	s_nop 0
	v_max_f32_e32 v140, v140, v140
	v_max_f32_e32 v141, v141, v141
	v_max_f32_e32 v140, v141, v140
	v_mov_b32_e32 v141, v140
	s_nop 1
	v_permlane32_swap_b32 v140, v141
	s_nop 0
	v_max3_f32 v141, v214, v140, v141
	v_cmp_neq_f32_e32 vcc, v141, v233
	s_nop 1
	v_cndmask_b32_e32 v184, 0, v141, vcc
	v_sub_f32_e32 v140, v214, v184
	v_exp_f32_e32 v140, v140
	v_mov_b32_e32 v214, v141
	v_pk_mul_f32 v[106:107], v[106:107], v[140:141] op_sel_hi:[1,0]
	v_pk_mul_f32 v[104:105], v[104:105], v[140:141] op_sel_hi:[1,0]
	v_pk_mul_f32 v[86:87], v[86:87], v[140:141] op_sel_hi:[1,0]
	v_pk_mul_f32 v[84:85], v[84:85], v[140:141] op_sel_hi:[1,0]
	v_pk_mul_f32 v[82:83], v[82:83], v[140:141] op_sel_hi:[1,0]
	v_pk_mul_f32 v[80:81], v[80:81], v[140:141] op_sel_hi:[1,0]
	v_pk_mul_f32 v[78:79], v[78:79], v[140:141] op_sel_hi:[1,0]
	v_pk_mul_f32 v[76:77], v[76:77], v[140:141] op_sel_hi:[1,0]
	v_pk_mul_f32 v[74:75], v[74:75], v[140:141] op_sel_hi:[1,0]
	v_pk_mul_f32 v[72:73], v[72:73], v[140:141] op_sel_hi:[1,0]
.LBB0_569:
	v_sub_f32_e32 v0, v0, v184
	v_sub_f32_e32 v1, v1, v184
	v_sub_f32_e32 v2, v2, v184
	v_sub_f32_e32 v3, v3, v184
	v_sub_f32_e32 v4, v4, v184
	v_sub_f32_e32 v5, v5, v184
	v_sub_f32_e32 v168, v6, v184
	v_sub_f32_e32 v169, v7, v184
	v_exp_f32_e32 v0, v0
	v_exp_f32_e32 v1, v1
	v_exp_f32_e32 v2, v2
	v_exp_f32_e32 v3, v3
	v_exp_f32_e32 v4, v4
	v_exp_f32_e32 v5, v5
	v_exp_f32_e32 v6, v168
	v_mov_b32_e32 v210, v184
	v_mov_b32_e32 v211, v214

.LBB0_571:
	s_xor_b64 s[10:11], s[10:11], -1
	s_add_i32 s5, s29, 0xffffffa0
	s_cmp_ge_i32 s5, s26
	s_cselect_b64 s[6:7], -1, 0
	s_cmp_lt_i32 s4, s28
	s_cselect_b64 s[4:5], -1, 0
	s_and_b64 s[4:5], s[6:7], s[4:5]
	s_andn2_b64 vcc, exec, s[4:5]
	s_cbranch_vccnz .LBB0_575
	ds_read_b128 v[140:143], v245 offset:4096
	ds_read_b128 v[144:147], v245 offset:4608
	ds_read_b128 v[152:155], v244 offset:4096
	ds_read_b128 v[148:151], v244 offset:4608
	v_add_u32_e32 v136, v215, v231
	ds_read_b128 v[124:127], v136 offset:16384
	ds_read_b128 v[128:131], v136 offset:18432
	ds_read_b128 v[132:135], v136 offset:20480
	ds_read_b128 v[136:139], v136 offset:22528
	s_waitcnt lgkmcnt(7)
	v_mfma_f32_16x16x32_bf16 v[0:3], v[140:143], v[24:27], 0
	s_add_i32 s4, s29, 63
	s_cmp_le_i32 s4, s22
	s_cselect_b64 s[18:19], -1, 0
	s_waitcnt lgkmcnt(6)
	v_mfma_f32_16x16x32_bf16 v[4:7], v[144:147], v[24:27], 0
	s_cmp_gt_i32 s4, s22
	s_mov_b64 s[20:21], -1
	s_waitcnt lgkmcnt(5)
	v_mfma_f32_16x16x32_bf16 v[160:163], v[152:155], v[28:31], v[0:3]
	s_waitcnt lgkmcnt(4)
	v_mfma_f32_16x16x32_bf16 v[156:159], v[148:151], v[28:31], v[4:7]
	s_cbranch_scc1 .LBB0_579
	s_add_i32 s4, s27, 0
	v_mov_b32_e32 v0, s4
	ds_read_b32 v0, v0 offset:49152
	v_cmp_eq_f32_e32 vcc, v243, v233
	s_waitcnt lgkmcnt(0)
	v_sub_f32_e32 v6, v212, v0
	v_fma_f32 v0, v160, s58, -v6
	v_fma_f32 v1, v161, s58, -v6
	v_fma_f32 v2, v162, s58, -v6
	v_fma_f32 v3, v163, s58, -v6
	v_fma_f32 v4, v156, s58, -v6
	v_fma_f32 v5, v157, s58, -v6
	v_fma_f32 v214, v158, s58, -v6
	v_fma_f32 v215, v159, s58, -v6
	v_max3_f32 v6, v0, v1, v2
	v_max3_f32 v7, v3, v4, v5
	s_nop 0
	v_max3_f32 v164, v214, v215, v215
	s_nop 0
	v_max3_f32 v6, v6, v7, v164
	v_cndmask_b32_e32 v7, v226, v233, vcc
	v_cmp_gt_f32_e32 vcc, v6, v7
	s_cbranch_vccz .LBB0_577
	v_add_f32_e32 v6, v212, v6
	v_mov_b32_e32 v7, v6
	s_nop 1
	v_permlane16_swap_b32 v7, v6
	s_nop 0
	v_max_f32_e32 v6, v6, v6
	v_max_f32_e32 v7, v7, v7
	v_max_f32_e32 v6, v7, v6
	v_mov_b32_e32 v7, v6
	s_nop 1
	v_permlane32_swap_b32 v6, v7
	s_nop 0
	v_max3_f32 v242, v243, v6, v7
	v_cmp_neq_f32_e32 vcc, v242, v233
	s_nop 1
	v_cndmask_b32_e32 v208, 0, v242, vcc
	v_sub_f32_e32 v6, v243, v208
	v_exp_f32_e32 v6, v6
	v_sub_f32_e32 v7, v208, v212
	v_sub_f32_e32 v0, v0, v7
	v_sub_f32_e32 v1, v1, v7
	v_pk_mul_f32 v[110:111], v[110:111], v[6:7] op_sel_hi:[1,0]
	v_pk_mul_f32 v[108:109], v[108:109], v[6:7] op_sel_hi:[1,0]
	v_pk_mul_f32 v[102:103], v[102:103], v[6:7] op_sel_hi:[1,0]
	v_pk_mul_f32 v[100:101], v[100:101], v[6:7] op_sel_hi:[1,0]
	v_pk_mul_f32 v[98:99], v[98:99], v[6:7] op_sel_hi:[1,0]
	v_pk_mul_f32 v[96:97], v[96:97], v[6:7] op_sel_hi:[1,0]
	v_pk_mul_f32 v[94:95], v[94:95], v[6:7] op_sel_hi:[1,0]
	v_pk_mul_f32 v[92:93], v[92:93], v[6:7] op_sel_hi:[1,0]
	v_pk_mul_f32 v[90:91], v[90:91], v[6:7] op_sel_hi:[1,0]
	v_pk_mul_f32 v[88:89], v[88:89], v[6:7] op_sel_hi:[1,0]
	v_sub_f32_e32 v2, v2, v7
	v_sub_f32_e32 v3, v3, v7
	v_sub_f32_e32 v4, v4, v7
	v_sub_f32_e32 v5, v5, v7
	v_sub_f32_e32 v214, v214, v7
	v_sub_f32_e32 v215, v215, v7
	s_branch .LBB0_578

.LBB0_579:
	s_and_b64 vcc, exec, s[20:21]
	s_cbranch_vccz .LBB0_583
	ds_read2_b32 v[0:1], v239 offset0:48 offset1:49
	ds_read2_b32 v[2:3], v239 offset0:50 offset1:51
	ds_read2_b32 v[4:5], v239 offset0:52 offset1:53
	ds_read2_b32 v[6:7], v239 offset0:54 offset1:55
	s_waitcnt lgkmcnt(3)
	v_fma_f32 v0, v160, s58, v0
	v_fma_f32 v1, v161, s58, v1
	s_waitcnt lgkmcnt(2)
	v_fma_f32 v2, v162, s58, v2
	v_fma_f32 v3, v163, s58, v3
	s_waitcnt lgkmcnt(1)
	v_fma_f32 v4, v156, s58, v4
	v_fma_f32 v5, v157, s58, v5
	v_max3_f32 v156, v0, v1, v2
	s_waitcnt lgkmcnt(0)
	v_fma_f32 v6, v158, s58, v6
	v_fma_f32 v7, v159, s58, v7
	v_max3_f32 v157, v3, v4, v5
	s_nop 0
	v_max3_f32 v158, v6, v7, v7
	s_nop 0
	v_max3_f32 v156, v156, v157, v158
	v_add_f32_e32 v157, 0x41800000, v243
	v_cmp_gt_f32_e32 vcc, v156, v157
	s_cbranch_vccz .LBB0_582
	v_mov_b32_e32 v157, v156
	s_nop 1
	v_permlane16_swap_b32 v157, v156
	s_nop 0
	v_max_f32_e32 v156, v156, v156
	v_max_f32_e32 v157, v157, v157
	v_max_f32_e32 v156, v157, v156
	v_mov_b32_e32 v157, v156
	s_nop 1
	v_permlane32_swap_b32 v157, v156
	s_nop 0
	v_max3_f32 v157, v243, v157, v156
	v_cmp_neq_f32_e32 vcc, v157, v233
	s_nop 1
	v_cndmask_b32_e32 v212, 0, v157, vcc
	v_sub_f32_e32 v156, v243, v212
	v_exp_f32_e32 v156, v156
	v_mov_b32_e32 v243, v157
	v_pk_mul_f32 v[110:111], v[110:111], v[156:157] op_sel_hi:[1,0]
	v_pk_mul_f32 v[108:109], v[108:109], v[156:157] op_sel_hi:[1,0]
	v_pk_mul_f32 v[102:103], v[102:103], v[156:157] op_sel_hi:[1,0]
	v_pk_mul_f32 v[100:101], v[100:101], v[156:157] op_sel_hi:[1,0]
	v_pk_mul_f32 v[98:99], v[98:99], v[156:157] op_sel_hi:[1,0]
	v_pk_mul_f32 v[96:97], v[96:97], v[156:157] op_sel_hi:[1,0]
	v_pk_mul_f32 v[94:95], v[94:95], v[156:157] op_sel_hi:[1,0]
	v_pk_mul_f32 v[92:93], v[92:93], v[156:157] op_sel_hi:[1,0]
	v_pk_mul_f32 v[90:91], v[90:91], v[156:157] op_sel_hi:[1,0]
	v_pk_mul_f32 v[88:89], v[88:89], v[156:157] op_sel_hi:[1,0]
.LBB0_582:
	v_sub_f32_e32 v0, v0, v212
	v_sub_f32_e32 v1, v1, v212
	v_sub_f32_e32 v2, v2, v212
	v_sub_f32_e32 v3, v3, v212
	v_sub_f32_e32 v4, v4, v212
	v_sub_f32_e32 v5, v5, v212
	v_sub_f32_e32 v214, v6, v212
	v_sub_f32_e32 v215, v7, v212
	v_exp_f32_e32 v0, v0
	v_exp_f32_e32 v1, v1
	v_exp_f32_e32 v2, v2
	v_exp_f32_e32 v3, v3
	v_exp_f32_e32 v4, v4
	v_exp_f32_e32 v5, v5
	v_exp_f32_e32 v6, v214
	v_mov_b32_e32 v208, v212
	v_mov_b32_e32 v242, v243
.LBB0_583:
	v_exp_f32_e32 v7, v215
	v_cvt_pk_bf16_f32 v0, v0, v1
	v_cvt_pk_bf16_f32 v1, v2, v3
	v_cvt_pk_bf16_f32 v2, v4, v5
	v_cvt_pk_bf16_f32 v3, v6, v7
	s_mov_b64 s[20:21], -1
	s_andn2_b64 vcc, exec, s[18:19]
	v_mfma_f32_16x16x32_bf16 v[108:111], v[112:115], v[0:3], v[108:111]
	s_waitcnt lgkmcnt(3)
	v_mfma_f32_16x16x32_bf16 v[100:103], v[124:127], v[0:3], v[100:103]
	s_waitcnt lgkmcnt(2)
	v_mfma_f32_16x16x32_bf16 v[96:99], v[128:131], v[0:3], v[96:99]
	s_waitcnt lgkmcnt(1)
	v_mfma_f32_16x16x32_bf16 v[92:95], v[132:135], v[0:3], v[92:95]
	s_waitcnt lgkmcnt(0)
	v_mfma_f32_16x16x32_bf16 v[88:91], v[136:139], v[0:3], v[88:91]
	v_mfma_f32_16x16x32_bf16 v[0:3], v[140:143], v[32:35], 0
	v_mfma_f32_16x16x32_bf16 v[152:155], v[152:155], v[36:39], v[0:3]
	v_mfma_f32_16x16x32_bf16 v[0:3], v[144:147], v[32:35], 0
	v_mfma_f32_16x16x32_bf16 v[140:143], v[148:151], v[36:39], v[0:3]
	s_cbranch_vccnz .LBB0_588
	s_add_i32 s4, s27, 0
	s_nop 4
	v_mov_b32_e32 v0, s4
	ds_read_b32 v0, v0 offset:49152
	v_cmp_eq_f32_e32 vcc, v211, v233
	s_waitcnt lgkmcnt(0)
	v_sub_f32_e32 v6, v210, v0
	v_fma_f32 v0, v152, s58, -v6
	v_fma_f32 v1, v153, s58, -v6
	v_fma_f32 v2, v154, s58, -v6
	v_fma_f32 v3, v155, s58, -v6
	v_fma_f32 v4, v140, s58, -v6
	v_fma_f32 v5, v141, s58, -v6
	v_fma_f32 v168, v142, s58, -v6
	v_fma_f32 v169, v143, s58, -v6
	v_max3_f32 v6, v0, v1, v2
	v_max3_f32 v7, v3, v4, v5
	s_nop 0
	v_max3_f32 v144, v168, v169, v169
	s_nop 0
	v_max3_f32 v6, v6, v7, v144
	v_cndmask_b32_e32 v7, v226, v233, vcc
	v_cmp_gt_f32_e32 vcc, v6, v7
	s_cbranch_vccz .LBB0_586
	v_add_f32_e32 v6, v210, v6
	v_mov_b32_e32 v7, v6
	s_nop 1
	v_permlane16_swap_b32 v6, v7
	s_nop 0
	v_max_f32_e32 v7, v7, v7
	v_max_f32_e32 v6, v6, v6
	v_max_f32_e32 v6, v6, v7
	v_mov_b32_e32 v7, v6
	s_nop 1
	v_permlane32_swap_b32 v7, v6
	s_nop 0
	v_max3_f32 v214, v211, v7, v6
	v_cmp_neq_f32_e32 vcc, v214, v233
	s_nop 1
	v_cndmask_b32_e32 v184, 0, v214, vcc
	v_sub_f32_e32 v6, v211, v184
	v_exp_f32_e32 v6, v6
	v_sub_f32_e32 v7, v184, v210
	v_sub_f32_e32 v0, v0, v7
	v_sub_f32_e32 v1, v1, v7
	v_pk_mul_f32 v[106:107], v[106:107], v[6:7] op_sel_hi:[1,0]
	v_pk_mul_f32 v[104:105], v[104:105], v[6:7] op_sel_hi:[1,0]
	v_pk_mul_f32 v[86:87], v[86:87], v[6:7] op_sel_hi:[1,0]
	v_pk_mul_f32 v[84:85], v[84:85], v[6:7] op_sel_hi:[1,0]
	v_pk_mul_f32 v[82:83], v[82:83], v[6:7] op_sel_hi:[1,0]
	v_pk_mul_f32 v[80:81], v[80:81], v[6:7] op_sel_hi:[1,0]
	v_pk_mul_f32 v[78:79], v[78:79], v[6:7] op_sel_hi:[1,0]
	v_pk_mul_f32 v[76:77], v[76:77], v[6:7] op_sel_hi:[1,0]
	v_pk_mul_f32 v[74:75], v[74:75], v[6:7] op_sel_hi:[1,0]
	v_pk_mul_f32 v[72:73], v[72:73], v[6:7] op_sel_hi:[1,0]
	v_sub_f32_e32 v2, v2, v7
	v_sub_f32_e32 v3, v3, v7
	v_sub_f32_e32 v4, v4, v7
	v_sub_f32_e32 v5, v5, v7
	v_sub_f32_e32 v168, v168, v7
	v_sub_f32_e32 v169, v169, v7
	s_branch .LBB0_587

.LBB0_588:
	s_and_b64 vcc, exec, s[20:21]
	s_cbranch_vccz .LBB0_592
	s_nop 3
	ds_read2_b32 v[0:1], v239 offset0:32 offset1:33
	ds_read2_b32 v[2:3], v239 offset0:34 offset1:35
	ds_read2_b32 v[4:5], v239 offset0:36 offset1:37
	ds_read2_b32 v[6:7], v239 offset0:38 offset1:39
	s_waitcnt lgkmcnt(3)
	v_fma_f32 v0, v152, s58, v0
	v_fma_f32 v1, v153, s58, v1
	s_waitcnt lgkmcnt(2)
	v_fma_f32 v2, v154, s58, v2
	v_fma_f32 v3, v155, s58, v3
	s_waitcnt lgkmcnt(1)
	v_fma_f32 v4, v140, s58, v4
	v_fma_f32 v5, v141, s58, v5
	v_max3_f32 v140, v0, v1, v2
	s_waitcnt lgkmcnt(0)
	v_fma_f32 v6, v142, s58, v6
	v_fma_f32 v7, v143, s58, v7
	v_max3_f32 v141, v3, v4, v5
	s_nop 0
	v_max3_f32 v142, v6, v7, v7
	s_nop 0
	v_max3_f32 v140, v140, v141, v142
	v_add_f32_e32 v141, 0x41800000, v211
	v_cmp_gt_f32_e32 vcc, v140, v141
	s_cbranch_vccz .LBB0_591
	v_mov_b32_e32 v141, v140
	s_nop 1
	v_permlane16_swap_b32 v141, v140
	s_nop 0
	v_max_f32_e32 v140, v140, v140
	v_max_f32_e32 v141, v141, v141
	v_max_f32_e32 v140, v141, v140
	v_mov_b32_e32 v141, v140
	s_nop 1
	v_permlane32_swap_b32 v141, v140
	s_nop 0
	v_max3_f32 v141, v211, v141, v140
	v_cmp_neq_f32_e32 vcc, v141, v233
	s_nop 1
	v_cndmask_b32_e32 v210, 0, v141, vcc
	v_sub_f32_e32 v140, v211, v210
	v_exp_f32_e32 v140, v140
	v_mov_b32_e32 v211, v141
	v_pk_mul_f32 v[106:107], v[106:107], v[140:141] op_sel_hi:[1,0]
	v_pk_mul_f32 v[104:105], v[104:105], v[140:141] op_sel_hi:[1,0]
	v_pk_mul_f32 v[86:87], v[86:87], v[140:141] op_sel_hi:[1,0]
	v_pk_mul_f32 v[84:85], v[84:85], v[140:141] op_sel_hi:[1,0]
	v_pk_mul_f32 v[82:83], v[82:83], v[140:141] op_sel_hi:[1,0]
	v_pk_mul_f32 v[80:81], v[80:81], v[140:141] op_sel_hi:[1,0]
	v_pk_mul_f32 v[78:79], v[78:79], v[140:141] op_sel_hi:[1,0]
	v_pk_mul_f32 v[76:77], v[76:77], v[140:141] op_sel_hi:[1,0]
	v_pk_mul_f32 v[74:75], v[74:75], v[140:141] op_sel_hi:[1,0]
	v_pk_mul_f32 v[72:73], v[72:73], v[140:141] op_sel_hi:[1,0]
.LBB0_591:
	v_sub_f32_e32 v0, v0, v210
	v_sub_f32_e32 v1, v1, v210
	v_sub_f32_e32 v2, v2, v210
	v_sub_f32_e32 v3, v3, v210
	v_sub_f32_e32 v4, v4, v210
	v_sub_f32_e32 v5, v5, v210
	v_sub_f32_e32 v168, v6, v210
	v_sub_f32_e32 v169, v7, v210
	v_exp_f32_e32 v0, v0
	v_exp_f32_e32 v1, v1
	v_exp_f32_e32 v2, v2
	v_exp_f32_e32 v3, v3
	v_exp_f32_e32 v4, v4
	v_exp_f32_e32 v5, v5
	v_exp_f32_e32 v6, v168
	v_mov_b32_e32 v184, v210
	v_mov_b32_e32 v214, v211

.LBB0_623:
	s_waitcnt vmcnt(0)
	v_mov_b32_e32 v96, 0x43e00000
	v_mul_f32_e32 v92, s60, v92
	v_mul_f32_e32 v93, s60, v93
	v_mul_f32_e32 v94, s60, v94
	v_mul_f32_e32 v95, s60, v95
	v_med3_f32 v97, v92, -v96, v96
	v_med3_f32 v93, v93, -v96, v96
	v_mov_b32_e32 v92, v185
	v_cvt_pk_fp8_f32 v92, v97, v93
	v_med3_f32 v94, v94, -v96, v96
	v_med3_f32 v95, v95, -v96, v96
	v_mul_f32_e32 v80, s60, v80
	v_mul_f32_e32 v81, s60, v81
	v_cvt_pk_fp8_f32 v92, v94, v95 op_sel:[0,0,1]
	v_mul_f32_e32 v88, s60, v88
	v_mul_f32_e32 v89, s60, v89
	v_mul_f32_e32 v84, s60, v84
	v_mul_f32_e32 v85, s60, v85
	v_med3_f32 v80, v80, -v96, v96
	v_med3_f32 v81, v81, -v96, v96
	v_mov_b32_e32 v95, v185
	v_ashrrev_i32_e32 v125, 31, v124
	v_med3_f32 v88, v88, -v96, v96
	v_med3_f32 v89, v89, -v96, v96
	v_mov_b32_e32 v93, v185
	v_med3_f32 v84, v84, -v96, v96
	v_med3_f32 v85, v85, -v96, v96
	v_mov_b32_e32 v94, v185
	v_cvt_pk_fp8_f32 v95, v80, v81
	v_lshlrev_b64 v[80:81], 10, v[124:125]
	s_lshl_b32 s40, s74, 6
	v_cvt_pk_fp8_f32 v93, v88, v89
	v_cvt_pk_fp8_f32 v94, v84, v85
	v_lshl_add_u64 v[80:81], s[86:87], 0, v[80:81]
	v_mov_b32_e32 v121, v185
	v_lshl_add_u64 v[80:81], v[80:81], 0, s[40:41]
	v_mul_f32_e32 v90, s60, v90
	v_mul_f32_e32 v91, s60, v91
	v_mul_f32_e32 v86, s60, v86
	v_mul_f32_e32 v87, s60, v87
	v_mul_f32_e32 v82, s60, v82
	v_mul_f32_e32 v83, s60, v83
	v_lshl_add_u64 v[80:81], v[80:81], 0, v[120:121]
	v_med3_f32 v90, v90, -v96, v96
	v_med3_f32 v91, v91, -v96, v96
	v_med3_f32 v86, v86, -v96, v96
	v_med3_f32 v87, v87, -v96, v96
	v_med3_f32 v82, v82, -v96, v96
	v_med3_f32 v83, v83, -v96, v96
	v_add_co_u32_e32 v80, vcc, s56, v80
	v_cvt_pk_fp8_f32 v93, v90, v91 op_sel:[0,0,1]
	v_cvt_pk_fp8_f32 v94, v86, v87 op_sel:[0,0,1]
	v_cvt_pk_fp8_f32 v95, v82, v83 op_sel:[0,0,1]
	v_addc_co_u32_e32 v81, vcc, 0, v81, vcc
	s_nop 1
	v_permlane16_swap_b32 v92, v93
	v_permlane16_swap_b32 v94, v95
	s_nop 1
	v_permlane32_swap_b32 v92, v94
	v_permlane32_swap_b32 v93, v95
	global_store_dwordx4 v[80:81], v[92:95], off offset:512
	v_mov_b32_e32 v80, 0x43e00000
	v_mul_f32_e32 v76, s60, v76
	v_mul_f32_e32 v77, s60, v77
	v_mul_f32_e32 v78, s60, v78
	v_mul_f32_e32 v79, s60, v79
	v_med3_f32 v81, v76, -v80, v80
	v_med3_f32 v77, v77, -v80, v80
	v_mov_b32_e32 v76, v185
	v_cvt_pk_fp8_f32 v76, v81, v77
	v_med3_f32 v78, v78, -v80, v80
	v_med3_f32 v79, v79, -v80, v80
	v_mul_f32_e32 v0, s60, v0
	v_mul_f32_e32 v1, s60, v1
	v_cvt_pk_fp8_f32 v76, v78, v79 op_sel:[0,0,1]
	v_mul_f32_e32 v72, s60, v72
	v_mul_f32_e32 v73, s60, v73
	v_mul_f32_e32 v4, s60, v4
	v_mul_f32_e32 v5, s60, v5
	v_med3_f32 v0, v0, -v80, v80
	v_med3_f32 v1, v1, -v80, v80
	v_mov_b32_e32 v79, v185
	v_ashrrev_i32_e32 v123, 31, v122
	v_med3_f32 v72, v72, -v80, v80
	v_med3_f32 v73, v73, -v80, v80
	v_mov_b32_e32 v77, v185
	v_med3_f32 v4, v4, -v80, v80
	v_med3_f32 v5, v5, -v80, v80
	v_mov_b32_e32 v78, v185
	v_cvt_pk_fp8_f32 v79, v0, v1
	v_lshlrev_b64 v[0:1], 10, v[122:123]
	v_cvt_pk_fp8_f32 v77, v72, v73
	v_cvt_pk_fp8_f32 v78, v4, v5
	v_lshl_add_u64 v[0:1], s[86:87], 0, v[0:1]
	v_lshl_add_u64 v[0:1], v[0:1], 0, s[40:41]
	v_mul_f32_e32 v74, s60, v74
	v_mul_f32_e32 v75, s60, v75
	v_mul_f32_e32 v6, s60, v6
	v_mul_f32_e32 v7, s60, v7
	v_mul_f32_e32 v2, s60, v2
	v_mul_f32_e32 v3, s60, v3
	v_lshl_add_u64 v[0:1], v[0:1], 0, v[120:121]
	v_med3_f32 v74, v74, -v80, v80
	v_med3_f32 v75, v75, -v80, v80
	v_med3_f32 v6, v6, -v80, v80
	v_med3_f32 v7, v7, -v80, v80
	v_med3_f32 v2, v2, -v80, v80
	v_med3_f32 v3, v3, -v80, v80
	v_add_co_u32_e32 v0, vcc, 0x72000000, v0
	v_cvt_pk_fp8_f32 v77, v74, v75 op_sel:[0,0,1]
	v_cvt_pk_fp8_f32 v78, v6, v7 op_sel:[0,0,1]
	v_cvt_pk_fp8_f32 v79, v2, v3 op_sel:[0,0,1]
	v_addc_co_u32_e32 v1, vcc, 0, v1, vcc
	s_nop 1
	v_permlane16_swap_b32 v76, v77
	v_permlane16_swap_b32 v78, v79
	s_nop 1
	v_permlane32_swap_b32 v76, v78
	v_permlane32_swap_b32 v77, v79
	global_store_dwordx4 v[0:1], v[76:79], off offset:512

.LBB0_633:
	s_lshl_b32 s9, s8, 13
	v_add_u32_e32 v116, s9, v198
	v_add_u32_e32 v212, s9, v199
	s_cmp_gt_i32 s23, s5
	v_add_u32_e32 v215, v116, v183
	v_add_u32_e32 v214, v116, v182
	v_add_u32_e32 v211, s23, v200
	s_cbranch_scc1 .LBB0_644
	ds_read_b128 v[136:139], v215
	ds_read_b128 v[140:143], v214
	ds_read_b128 v[144:147], v215 offset:512
	ds_read_b128 v[148:151], v214 offset:512
	v_add_u32_e32 v128, v212, v183
	s_waitcnt lgkmcnt(3)
	v_mfma_f32_16x16x32_bf16 v[116:119], v[136:139], v[24:27], 0
	ds_read_b128 v[132:135], v184
	ds_read_b128 v[152:155], v184 offset:16
	s_add_i32 s9, s23, 31
	s_cmp_ge_i32 s9, s22
	s_waitcnt lgkmcnt(3)
	v_mfma_f32_16x16x32_bf16 v[174:177], v[144:147], v[24:27], 0
	s_cselect_b64 s[18:19], -1, 0
	s_cmp_lt_i32 s9, s22
	v_mfma_f32_16x16x32_bf16 v[188:191], v[140:143], v[28:31], v[116:119]
	s_nop 2
	ds_read_b128 v[116:119], v128 offset:16384
	ds_read_b128 v[120:123], v128 offset:18432
	ds_read_b128 v[124:127], v128 offset:20480
	ds_read_b128 v[128:131], v128 offset:22528
	s_waitcnt lgkmcnt(5)
	v_fma_f32 v180, v188, s58, v132
	v_fma_f32 v181, v189, s58, v133
	v_mfma_f32_16x16x32_bf16 v[176:179], v[148:151], v[28:31], v[174:177]
	s_waitcnt lgkmcnt(4)
	s_nop 6
	v_fma_f32 v174, v178, s58, v154
	v_fma_f32 v175, v179, s58, v155
	v_fma_f32 v178, v190, s58, v134
	v_fma_f32 v179, v191, s58, v135
	v_fma_f32 v176, v176, s58, v152
	v_fma_f32 v177, v177, s58, v153
	s_cbranch_scc1 .LBB0_636
	v_cmp_gt_i32_e32 vcc, v211, v158
	s_nop 1
	v_cndmask_b32_e32 v187, v180, v196, vcc
	v_cmp_lt_i32_e32 vcc, v211, v158
	s_nop 1
	v_cndmask_b32_e32 v180, v187, v180, vcc
	v_add_u32_e32 v187, 2, v211
	v_cndmask_b32_e32 v181, v196, v181, vcc
	v_cmp_gt_i32_e32 vcc, v187, v158
	v_add_u32_e32 v187, 3, v211
	s_nop 0
	v_cndmask_b32_e32 v178, v178, v196, vcc
	v_cmp_gt_i32_e32 vcc, v187, v158
	v_add_u32_e32 v187, 4, v211
	s_nop 0
	v_cndmask_b32_e32 v179, v179, v196, vcc
	v_cmp_gt_i32_e32 vcc, v187, v158
	v_add_u32_e32 v187, 5, v211
	s_nop 0
	v_cndmask_b32_e32 v176, v176, v196, vcc
	v_cmp_gt_i32_e32 vcc, v187, v158
	v_add_u32_e32 v187, 6, v211
	s_nop 0
	v_cndmask_b32_e32 v177, v177, v196, vcc
	v_cmp_gt_i32_e32 vcc, v187, v158
	v_add_u32_e32 v187, 7, v211
	s_nop 0
	v_cndmask_b32_e32 v174, v174, v196, vcc
	v_cmp_gt_i32_e32 vcc, v187, v158
	s_nop 1
	v_cndmask_b32_e32 v175, v175, v196, vcc

.LBB0_638:
	v_mfma_f32_16x16x32_bf16 v[136:139], v[136:139], v[32:35], 0
	v_add_f32_e64 v180, v180, -v172
	v_add_f32_e64 v181, v181, -v172
	v_sub_f32_e32 v178, v178, v172
	v_sub_f32_e32 v179, v179, v172
	v_sub_f32_e32 v176, v176, v172
	v_sub_f32_e32 v177, v177, v172
	v_sub_f32_e32 v174, v174, v172
	v_sub_f32_e32 v175, v175, v172
	v_exp_f32_e32 v180, v180
	v_exp_f32_e32 v181, v181
	v_exp_f32_e32 v178, v178
	v_exp_f32_e32 v179, v179
	v_exp_f32_e32 v176, v176
	v_exp_f32_e32 v177, v177
	v_exp_f32_e32 v187, v174
	v_exp_f32_e32 v188, v175
	v_mfma_f32_16x16x32_bf16 v[140:143], v[140:143], v[36:39], v[136:139]
	v_cvt_pk_bf16_f32 v174, v180, v181
	v_cvt_pk_bf16_f32 v175, v178, v179
	v_cvt_pk_bf16_f32 v176, v176, v177
	v_mfma_f32_16x16x32_bf16 v[136:139], v[144:147], v[32:35], 0
	v_cvt_pk_bf16_f32 v177, v187, v188
	s_nop 2
	v_fma_f32 v132, v140, s58, v132
	v_fma_f32 v133, v141, s58, v133
	s_andn2_b64 vcc, exec, s[18:19]
	v_mfma_f32_16x16x32_bf16 v[144:147], v[148:151], v[36:39], v[136:139]
	v_mfma_f32_16x16x32_bf16 v[100:103], v[104:107], v[174:177], v[100:103]
	s_nop 1
	v_fma_f32 v138, v142, s58, v134
	v_fma_f32 v139, v143, s58, v135
	s_nop 2
	v_fma_f32 v136, v146, s58, v154
	v_fma_f32 v137, v147, s58, v155
	v_fma_f32 v134, v144, s58, v152
	v_fma_f32 v135, v145, s58, v153
	s_waitcnt lgkmcnt(3)
	v_mfma_f32_16x16x32_bf16 v[92:95], v[116:119], v[174:177], v[92:95]
	s_waitcnt lgkmcnt(2)
	v_mfma_f32_16x16x32_bf16 v[88:91], v[120:123], v[174:177], v[88:91]
	s_waitcnt lgkmcnt(1)
	v_mfma_f32_16x16x32_bf16 v[84:87], v[124:127], v[174:177], v[84:87]
	s_waitcnt lgkmcnt(0)
	v_mfma_f32_16x16x32_bf16 v[80:83], v[128:131], v[174:177], v[80:83]
	s_cbranch_vccnz .LBB0_640
	v_cmp_gt_i32_e32 vcc, v211, v156
	s_nop 1
	v_cndmask_b32_e32 v140, v132, v196, vcc
	v_cmp_lt_i32_e32 vcc, v211, v156
	s_nop 1
	v_cndmask_b32_e32 v132, v140, v132, vcc
	v_cndmask_b32_e32 v133, v196, v133, vcc
	v_cmp_gt_i32_e32 vcc, v211, v201
	s_nop 1
	v_cndmask_b32_e32 v138, v138, v196, vcc
	v_cmp_gt_i32_e32 vcc, v211, v202
	s_nop 1
	v_cndmask_b32_e32 v139, v139, v196, vcc
	v_cmp_gt_i32_e32 vcc, v211, v203
	s_nop 1
	v_cndmask_b32_e32 v134, v134, v196, vcc
	v_cmp_gt_i32_e32 vcc, v211, v204
	s_nop 1
	v_cndmask_b32_e32 v135, v135, v196, vcc
	v_cmp_gt_i32_e32 vcc, v211, v205
	s_nop 1
	v_cndmask_b32_e32 v136, v136, v196, vcc
	v_cmp_gt_i32_e32 vcc, v211, v206
	s_nop 1
	v_cndmask_b32_e32 v137, v137, v196, vcc

.LBB0_642:
	v_sub_f32_e32 v132, v132, v170
	v_sub_f32_e32 v133, v133, v170
	s_nop 0
	v_exp_f32_e32 v140, v132
	v_exp_f32_e32 v141, v133
	v_sub_f32_e32 v132, v138, v170
	v_sub_f32_e32 v133, v139, v170
	s_nop 0
	v_exp_f32_e32 v138, v132
	v_exp_f32_e32 v139, v133
	v_sub_f32_e32 v132, v134, v170
	v_sub_f32_e32 v133, v135, v170
	s_nop 0
	v_exp_f32_e32 v134, v132
	v_exp_f32_e32 v135, v133
	v_sub_f32_e32 v132, v136, v170
	v_sub_f32_e32 v133, v137, v170
	v_cvt_pk_bf16_f32 v134, v134, v135
	v_exp_f32_e32 v136, v132
	v_exp_f32_e32 v137, v133
	v_cvt_pk_bf16_f32 v132, v140, v141
	v_cvt_pk_bf16_f32 v133, v138, v139
	v_cvt_pk_bf16_f32 v135, v136, v137
	s_nop 1
	v_mfma_f32_16x16x32_bf16 v[96:99], v[104:107], v[132:135], v[96:99]
	v_mfma_f32_16x16x32_bf16 v[76:79], v[116:119], v[132:135], v[76:79]
	v_mfma_f32_16x16x32_bf16 v[72:75], v[120:123], v[132:135], v[72:75]
	v_mfma_f32_16x16x32_bf16 v[4:7], v[124:127], v[132:135], v[4:7]
	v_mfma_f32_16x16x32_bf16 v[0:3], v[128:131], v[132:135], v[0:3]
	s_add_i32 s9, s23, 32
	s_cmp_gt_i32 s9, s5
	s_cbranch_scc0 .LBB0_645

.LBB0_645:
	ds_read_b128 v[140:143], v215 offset:4096
	ds_read_b128 v[144:147], v215 offset:4608
	ds_read_b128 v[152:155], v214 offset:4096
	ds_read_b128 v[148:151], v214 offset:4608
	v_add_u32_e32 v128, v212, v182
	s_waitcnt lgkmcnt(3)
	v_mfma_f32_16x16x32_bf16 v[124:127], v[140:143], v[24:27], 0
	ds_read_b128 v[132:135], v184 offset:128
	ds_read_b128 v[136:139], v184 offset:144
	ds_read_b128 v[116:119], v128 offset:16384
	ds_read_b128 v[120:123], v128 offset:18432
	s_add_i32 s9, s23, 63
	s_waitcnt lgkmcnt(6)
	v_mfma_f32_16x16x32_bf16 v[174:177], v[144:147], v[24:27], 0
	s_cmp_ge_i32 s9, s22
	s_cselect_b64 s[18:19], -1, 0
	s_cmp_lt_i32 s9, s22
	s_waitcnt lgkmcnt(5)
	v_mfma_f32_16x16x32_bf16 v[188:191], v[152:155], v[28:31], v[124:127]
	s_nop 2
	ds_read_b128 v[124:127], v128 offset:20480
	ds_read_b128 v[128:131], v128 offset:22528
	v_add_u32_e32 v212, 32, v211
	s_waitcnt lgkmcnt(5)
	s_nop 0
	v_fma_f32 v180, v188, s58, v132
	v_fma_f32 v181, v189, s58, v133
	v_mfma_f32_16x16x32_bf16 v[176:179], v[148:151], v[28:31], v[174:177]
	s_waitcnt lgkmcnt(4)
	s_nop 6
	v_fma_f32 v174, v178, s58, v138
	v_fma_f32 v175, v179, s58, v139
	v_fma_f32 v178, v190, s58, v134
	v_fma_f32 v179, v191, s58, v135
	v_fma_f32 v176, v176, s58, v136
	v_fma_f32 v177, v177, s58, v137
	s_cbranch_scc1 .LBB0_647
	v_cmp_gt_i32_e32 vcc, v212, v158
	s_nop 1
	v_cndmask_b32_e32 v187, v180, v196, vcc
	v_cmp_lt_i32_e32 vcc, v212, v158
	s_nop 1
	v_cndmask_b32_e32 v180, v187, v180, vcc
	v_add_u32_e32 v187, 34, v211
	v_cndmask_b32_e32 v181, v196, v181, vcc
	v_cmp_gt_i32_e32 vcc, v187, v158
	v_add_u32_e32 v187, 35, v211
	s_nop 0
	v_cndmask_b32_e32 v178, v178, v196, vcc
	v_cmp_gt_i32_e32 vcc, v187, v158
	v_add_u32_e32 v187, 36, v211
	s_nop 0
	v_cndmask_b32_e32 v179, v179, v196, vcc
	v_cmp_gt_i32_e32 vcc, v187, v158
	v_add_u32_e32 v187, 37, v211
	s_nop 0
	v_cndmask_b32_e32 v176, v176, v196, vcc
	v_cmp_gt_i32_e32 vcc, v187, v158
	v_add_u32_e32 v187, 38, v211
	s_nop 0
	v_cndmask_b32_e32 v177, v177, v196, vcc
	v_cmp_gt_i32_e32 vcc, v187, v158
	v_add_u32_e32 v187, 39, v211
	s_nop 0
	v_cndmask_b32_e32 v174, v174, v196, vcc
	v_cmp_gt_i32_e32 vcc, v187, v158
	s_nop 1
	v_cndmask_b32_e32 v175, v175, v196, vcc

.LBB0_649:
	v_mfma_f32_16x16x32_bf16 v[140:143], v[140:143], v[32:35], 0
	v_add_f32_e64 v180, v180, -v172
	v_add_f32_e64 v181, v181, -v172
	v_sub_f32_e32 v178, v178, v172
	v_sub_f32_e32 v179, v179, v172
	v_sub_f32_e32 v176, v176, v172
	v_sub_f32_e32 v177, v177, v172
	v_sub_f32_e32 v174, v174, v172
	v_sub_f32_e32 v175, v175, v172
	v_exp_f32_e32 v180, v180
	v_exp_f32_e32 v181, v181
	v_exp_f32_e32 v178, v178
	v_exp_f32_e32 v179, v179
	v_exp_f32_e32 v176, v176
	v_exp_f32_e32 v177, v177
	v_exp_f32_e32 v187, v174
	v_exp_f32_e32 v188, v175
	v_mfma_f32_16x16x32_bf16 v[152:155], v[152:155], v[36:39], v[140:143]
	v_cvt_pk_bf16_f32 v174, v180, v181
	v_cvt_pk_bf16_f32 v175, v178, v179
	v_cvt_pk_bf16_f32 v176, v176, v177
	v_mfma_f32_16x16x32_bf16 v[140:143], v[144:147], v[32:35], 0
	v_cvt_pk_bf16_f32 v177, v187, v188
	s_nop 2
	v_fma_f32 v132, v152, s58, v132
	v_fma_f32 v133, v153, s58, v133
	s_andn2_b64 vcc, exec, s[18:19]
	v_mfma_f32_16x16x32_bf16 v[142:145], v[148:151], v[36:39], v[140:143]
	v_mfma_f32_16x16x32_bf16 v[100:103], v[104:107], v[174:177], v[100:103]
	s_nop 1
	v_fma_f32 v140, v154, s58, v134
	v_fma_f32 v141, v155, s58, v135
	s_nop 2
	v_fma_f32 v138, v144, s58, v138
	v_fma_f32 v139, v145, s58, v139
	v_fma_f32 v134, v142, s58, v136
	v_fma_f32 v135, v143, s58, v137
	s_waitcnt lgkmcnt(3)
	v_mfma_f32_16x16x32_bf16 v[92:95], v[116:119], v[174:177], v[92:95]
	s_waitcnt lgkmcnt(2)
	v_mfma_f32_16x16x32_bf16 v[88:91], v[120:123], v[174:177], v[88:91]
	s_waitcnt lgkmcnt(1)
	v_mfma_f32_16x16x32_bf16 v[84:87], v[124:127], v[174:177], v[84:87]
	s_waitcnt lgkmcnt(0)
	v_mfma_f32_16x16x32_bf16 v[80:83], v[128:131], v[174:177], v[80:83]
	s_cbranch_vccnz .LBB0_651
	v_cmp_gt_i32_e32 vcc, v212, v156
	s_nop 1
	v_cndmask_b32_e32 v136, v132, v196, vcc
	v_cmp_lt_i32_e32 vcc, v212, v156
	s_nop 1
	v_cndmask_b32_e32 v132, v136, v132, vcc
	v_cndmask_b32_e32 v133, v196, v133, vcc
	v_cmp_gt_i32_e32 vcc, v212, v201
	s_nop 1
	v_cndmask_b32_e32 v140, v140, v196, vcc
	v_cmp_gt_i32_e32 vcc, v212, v202
	s_nop 1
	v_cndmask_b32_e32 v141, v141, v196, vcc
	v_cmp_gt_i32_e32 vcc, v212, v203
	s_nop 1
	v_cndmask_b32_e32 v134, v134, v196, vcc
	v_cmp_gt_i32_e32 vcc, v212, v204
	s_nop 1
	v_cndmask_b32_e32 v135, v135, v196, vcc
	v_cmp_gt_i32_e32 vcc, v212, v205
	s_nop 1
	v_cndmask_b32_e32 v138, v138, v196, vcc
	v_cmp_gt_i32_e32 vcc, v212, v206
	s_nop 1
	v_cndmask_b32_e32 v139, v139, v196, vcc

.LBB0_653:
	v_sub_f32_e32 v132, v132, v170
	v_sub_f32_e32 v133, v133, v170
	s_nop 0
	v_exp_f32_e32 v136, v132
	v_exp_f32_e32 v137, v133
	v_sub_f32_e32 v132, v140, v170
	v_sub_f32_e32 v133, v141, v170
	s_nop 0
	v_exp_f32_e32 v140, v132
	v_exp_f32_e32 v141, v133
	v_sub_f32_e32 v132, v134, v170
	v_sub_f32_e32 v133, v135, v170
	s_nop 0
	v_exp_f32_e32 v134, v132
	v_exp_f32_e32 v135, v133
	v_sub_f32_e32 v132, v138, v170
	v_sub_f32_e32 v133, v139, v170
	v_cvt_pk_bf16_f32 v134, v134, v135
	v_exp_f32_e32 v138, v132
	v_exp_f32_e32 v139, v133
	v_cvt_pk_bf16_f32 v132, v136, v137
	v_cvt_pk_bf16_f32 v133, v140, v141
	v_cvt_pk_bf16_f32 v135, v138, v139
	s_nop 1
	v_mfma_f32_16x16x32_bf16 v[96:99], v[104:107], v[132:135], v[96:99]
	v_mfma_f32_16x16x32_bf16 v[76:79], v[116:119], v[132:135], v[76:79]
	v_mfma_f32_16x16x32_bf16 v[72:75], v[120:123], v[132:135], v[72:75]
	v_mfma_f32_16x16x32_bf16 v[4:7], v[124:127], v[132:135], v[4:7]
	v_mfma_f32_16x16x32_bf16 v[0:3], v[128:131], v[132:135], v[0:3]
	s_andn2_b64 vcc, exec, s[16:17]
	s_mov_b64 s[16:17], -1
	s_cbranch_vccnz .LBB0_628

.LBB0_667:
	s_lshl_b32 s19, s4, 13
	v_add_u32_e32 v100, s19, v170
	v_add_u32_e32 v178, v100, v166
	v_add_u32_e32 v176, v100, v155
	ds_read_b128 v[116:119], v178
	ds_read_b128 v[120:123], v178 offset:512
	ds_read_b128 v[124:127], v176
	ds_read_b128 v[128:131], v176 offset:512
	s_waitcnt lgkmcnt(3)
	v_mfma_f32_16x16x32_bf16 v[100:103], v[116:119], v[24:27], 0
	v_add_u32_e32 v177, s19, v171
	v_add_u32_e32 v112, v177, v166
	v_cmp_eq_f32_e32 vcc, v175, v167
	s_waitcnt lgkmcnt(2)
	v_mfma_f32_16x16x32_bf16 v[158:161], v[120:123], v[24:27], 0
	s_waitcnt lgkmcnt(1)
	v_mfma_f32_16x16x32_bf16 v[162:165], v[124:127], v[28:31], v[100:103]
	s_nop 2
	ds_read_b128 v[100:103], v112 offset:16384
	ds_read_b128 v[104:107], v112 offset:18432
	ds_read_b128 v[108:111], v112 offset:20480
	ds_read_b128 v[112:115], v112 offset:22528
	s_waitcnt lgkmcnt(4)
	v_mfma_f32_16x16x32_bf16 v[180:183], v[128:131], v[28:31], v[158:161]
	s_nop 2
	v_fma_f32 v158, v162, s58, -v154
	v_fma_f32 v159, v163, s58, -v154
	v_fma_f32 v160, v164, s58, -v154
	v_fma_f32 v161, v165, s58, -v154
	s_nop 1
	v_fma_f32 v162, v180, s58, -v154
	v_fma_f32 v163, v181, s58, -v154
	v_max3_f32 v179, v158, v159, v160
	v_fma_f32 v164, v182, s58, -v154
	v_fma_f32 v165, v183, s58, -v154
	v_max3_f32 v180, v161, v162, v163
	s_nop 0
	v_max3_f32 v181, v164, v165, v165
	s_nop 0
	v_max3_f32 v179, v179, v180, v181
	v_cndmask_b32_e32 v180, v226, v167, vcc
	v_cmp_gt_f32_e32 vcc, v179, v180
	s_cbranch_vccz .LBB0_669
	v_add_f32_e32 v179, v154, v179
	v_mov_b32_e32 v180, v179
	s_nop 1
	v_permlane16_swap_b32 v180, v179
	s_nop 0
	v_max_f32_e32 v179, v179, v179
	v_max_f32_e32 v180, v180, v180
	v_max_f32_e32 v179, v180, v179
	v_mov_b32_e32 v180, v179
	s_nop 1
	v_permlane32_swap_b32 v180, v179
	s_nop 0
	v_max3_f32 v179, v175, v180, v179
	v_cmp_neq_f32_e32 vcc, v179, v167
	s_nop 1
	v_cndmask_b32_e32 v181, 0, v179, vcc
	v_sub_f32_e32 v175, v175, v181
	v_exp_f32_e32 v180, v175
	v_sub_f32_e32 v154, v181, v154
	v_sub_f32_e32 v158, v158, v154
	v_sub_f32_e32 v159, v159, v154
	v_pk_mul_f32 v[98:99], v[98:99], v[180:181] op_sel_hi:[1,0]
	v_pk_mul_f32 v[96:97], v[96:97], v[180:181] op_sel_hi:[1,0]
	v_pk_mul_f32 v[94:95], v[94:95], v[180:181] op_sel_hi:[1,0]
	v_pk_mul_f32 v[92:93], v[92:93], v[180:181] op_sel_hi:[1,0]
	v_pk_mul_f32 v[90:91], v[90:91], v[180:181] op_sel_hi:[1,0]
	v_pk_mul_f32 v[88:89], v[88:89], v[180:181] op_sel_hi:[1,0]
	v_pk_mul_f32 v[78:79], v[78:79], v[180:181] op_sel_hi:[1,0]
	v_pk_mul_f32 v[76:77], v[76:77], v[180:181] op_sel_hi:[1,0]
	v_pk_mul_f32 v[74:75], v[74:75], v[180:181] op_sel_hi:[1,0]
	v_pk_mul_f32 v[72:73], v[72:73], v[180:181] op_sel_hi:[1,0]
	v_sub_f32_e32 v160, v160, v154
	v_sub_f32_e32 v161, v161, v154
	v_sub_f32_e32 v162, v162, v154
	v_sub_f32_e32 v163, v163, v154
	v_sub_f32_e32 v164, v164, v154
	v_sub_f32_e32 v165, v165, v154
	v_mov_b32_e32 v175, v179
	v_mov_b32_e32 v154, v181
.LBB0_669:
	v_mfma_f32_16x16x32_bf16 v[116:119], v[116:119], v[32:35], 0
	v_exp_f32_e32 v158, v158
	v_exp_f32_e32 v159, v159
	v_exp_f32_e32 v160, v160
	v_mfma_f32_16x16x32_bf16 v[120:123], v[120:123], v[32:35], 0
	v_exp_f32_e32 v161, v161
	v_exp_f32_e32 v162, v162
	v_exp_f32_e32 v163, v163
	v_exp_f32_e32 v164, v164
	v_exp_f32_e32 v165, v165
	s_waitcnt vmcnt(0)
	v_lshrrev_b64 v[188:189], v136, v[156:157]
	v_bfe_i32 v179, v188, 0, 1
	v_bfe_i32 v180, v188, 1, 1
	v_bfe_i32 v181, v188, 2, 1
	v_bfe_i32 v182, v188, 3, 1
	v_bfe_i32 v183, v188, 4, 1
	v_bfe_i32 v196, v188, 5, 1
	v_bfe_i32 v197, v188, 6, 1
	v_bfe_i32 v198, v188, 7, 1
	v_mfma_f32_16x16x32_bf16 v[116:119], v[124:127], v[36:39], v[116:119]
	v_and_b32_e32 v187, 0xffff, v179
	v_and_b32_e32 v189, 0xffff0000, v180
	v_and_b32_e32 v190, 0xffff, v181
	v_mfma_f32_16x16x32_bf16 v[120:123], v[128:131], v[36:39], v[120:123]
	v_and_b32_e32 v191, 0xffff0000, v182
	v_and_b32_e32 v192, 0xffff, v183
	v_and_b32_e32 v193, 0xffff0000, v196
	v_and_b32_e32 v199, 0xffff, v197
	v_and_b32_e32 v188, 0xffff0000, v198
	v_cvt_pk_bf16_f32 v158, v158, v159
	v_cvt_pk_bf16_f32 v159, v160, v161
	v_cvt_pk_bf16_f32 v160, v162, v163
	v_cvt_pk_bf16_f32 v161, v164, v165
	v_bitop3_b32 v158, v189, v158, v187 bitop3:0xc8
	v_bitop3_b32 v159, v191, v159, v190 bitop3:0xc8
	v_bitop3_b32 v160, v193, v160, v192 bitop3:0xc8
	v_bitop3_b32 v161, v188, v161, v199 bitop3:0xc8
	v_fma_f32 v116, v116, s58, -v152
	v_fma_f32 v117, v117, s58, -v152
	v_fma_f32 v118, v118, s58, -v152
	v_fma_f32 v119, v119, s58, -v152
	v_mfma_f32_16x16x32_bf16 v[96:99], v[64:67], v[158:161], v[96:99]
	v_fma_f32 v120, v120, s58, -v152
	v_fma_f32 v121, v121, s58, -v152
	v_max3_f32 v124, v116, v117, v118
	v_cmp_eq_f32_e32 vcc, v174, v167
	s_waitcnt lgkmcnt(3)
	v_mfma_f32_16x16x32_bf16 v[92:95], v[100:103], v[158:161], v[92:95]
	v_max3_f32 v125, v119, v120, v121
	v_fma_f32 v122, v122, s58, -v152
	v_fma_f32 v123, v123, s58, -v152
	s_waitcnt lgkmcnt(2)
	v_mfma_f32_16x16x32_bf16 v[88:91], v[104:107], v[158:161], v[88:91]
	v_max3_f32 v126, v122, v123, v123
	s_nop 0
	v_max3_f32 v124, v124, v125, v126
	s_waitcnt lgkmcnt(1)
	v_mfma_f32_16x16x32_bf16 v[76:79], v[108:111], v[158:161], v[76:79]
	v_cndmask_b32_e32 v125, v226, v167, vcc
	v_cmp_gt_f32_e32 vcc, v124, v125
	s_waitcnt lgkmcnt(0)
	v_mfma_f32_16x16x32_bf16 v[72:75], v[112:115], v[158:161], v[72:75]
	s_cbranch_vccz .LBB0_671
	v_add_f32_e32 v124, v152, v124
	v_mov_b32_e32 v125, v124
	s_nop 1
	v_permlane16_swap_b32 v125, v124
	s_nop 0
	v_max_f32_e32 v124, v124, v124
	v_max_f32_e32 v125, v125, v125
	v_max_f32_e32 v124, v125, v124
	v_mov_b32_e32 v125, v124
	s_nop 1
	v_permlane32_swap_b32 v124, v125
	s_nop 0
	v_max3_f32 v125, v174, v124, v125
	v_cmp_neq_f32_e32 vcc, v125, v167
	s_nop 1
	v_cndmask_b32_e32 v126, 0, v125, vcc
	v_sub_f32_e32 v124, v174, v126
	v_exp_f32_e32 v124, v124
	v_sub_f32_e32 v127, v126, v152
	v_sub_f32_e32 v116, v116, v127
	v_sub_f32_e32 v117, v117, v127
	v_pk_mul_f32 v[70:71], v[70:71], v[124:125] op_sel_hi:[1,0]
	v_pk_mul_f32 v[68:69], v[68:69], v[124:125] op_sel_hi:[1,0]
	v_pk_mul_f32 v[62:63], v[62:63], v[124:125] op_sel_hi:[1,0]
	v_pk_mul_f32 v[60:61], v[60:61], v[124:125] op_sel_hi:[1,0]
	v_pk_mul_f32 v[58:59], v[58:59], v[124:125] op_sel_hi:[1,0]
	v_pk_mul_f32 v[56:57], v[56:57], v[124:125] op_sel_hi:[1,0]
	v_pk_mul_f32 v[6:7], v[6:7], v[124:125] op_sel_hi:[1,0]
	v_pk_mul_f32 v[4:5], v[4:5], v[124:125] op_sel_hi:[1,0]
	v_pk_mul_f32 v[2:3], v[2:3], v[124:125] op_sel_hi:[1,0]
	v_pk_mul_f32 v[0:1], v[0:1], v[124:125] op_sel_hi:[1,0]
	v_sub_f32_e32 v118, v118, v127
	v_sub_f32_e32 v119, v119, v127
	v_sub_f32_e32 v120, v120, v127
	v_sub_f32_e32 v121, v121, v127
	v_sub_f32_e32 v122, v122, v127
	v_sub_f32_e32 v123, v123, v127
	v_mov_b32_e32 v174, v125
	v_mov_b32_e32 v152, v126
.LBB0_671:
	v_exp_f32_e32 v116, v116
	v_exp_f32_e32 v117, v117
	v_exp_f32_e32 v118, v118
	v_exp_f32_e32 v119, v119
	v_exp_f32_e32 v120, v120
	v_exp_f32_e32 v121, v121
	v_exp_f32_e32 v122, v122
	v_exp_f32_e32 v123, v123
	v_bfi_b32 v124, s45, v180, v179
	v_bfi_b32 v125, s45, v182, v181
	v_bfi_b32 v126, s45, v196, v183
	v_bfi_b32 v127, s45, v198, v197
	v_cvt_pk_bf16_f32 v116, v116, v117
	v_cvt_pk_bf16_f32 v117, v118, v119
	v_cvt_pk_bf16_f32 v118, v120, v121
	v_cvt_pk_bf16_f32 v119, v122, v123
	v_and_b32_e32 v116, v124, v116
	v_and_b32_e32 v117, v125, v117
	v_and_b32_e32 v118, v126, v118
	v_and_b32_e32 v119, v127, v119
	v_cmp_eq_f32_e32 vcc, v175, v167
	s_nop 0
	v_mfma_f32_16x16x32_bf16 v[68:71], v[64:67], v[116:119], v[68:71]
	v_mfma_f32_16x16x32_bf16 v[60:63], v[100:103], v[116:119], v[60:63]
	v_mfma_f32_16x16x32_bf16 v[56:59], v[104:107], v[116:119], v[56:59]
	v_mfma_f32_16x16x32_bf16 v[4:7], v[108:111], v[116:119], v[4:7]
	v_mfma_f32_16x16x32_bf16 v[0:3], v[112:115], v[116:119], v[0:3]
	ds_read_b128 v[120:123], v178 offset:4096
	ds_read_b128 v[116:119], v178 offset:4608
	ds_read_b128 v[128:131], v176 offset:4096
	ds_read_b128 v[124:127], v176 offset:4608
	s_waitcnt lgkmcnt(3)
	v_mfma_f32_16x16x32_bf16 v[100:103], v[120:123], v[24:27], 0
	s_waitcnt lgkmcnt(2)
	v_mfma_f32_16x16x32_bf16 v[162:165], v[116:119], v[24:27], 0
	s_waitcnt lgkmcnt(1)
	v_mfma_f32_16x16x32_bf16 v[158:161], v[128:131], v[28:31], v[100:103]
	s_nop 3
	v_add_u32_e32 v100, v177, v155
	ds_read_b128 v[104:107], v100 offset:16384
	ds_read_b128 v[108:111], v100 offset:18432
	ds_read_b128 v[112:115], v100 offset:20480
	ds_read_b128 v[100:103], v100 offset:22528
	s_waitcnt lgkmcnt(4)
	v_mfma_f32_16x16x32_bf16 v[162:165], v[124:127], v[28:31], v[162:165]
	v_fma_f32 v158, v158, s58, -v154
	v_fma_f32 v159, v159, s58, -v154
	v_fma_f32 v160, v160, s58, -v154
	v_fma_f32 v161, v161, s58, -v154
	s_nop 0
	v_max3_f32 v176, v158, v159, v160
	s_nop 3
	v_fma_f32 v162, v162, s58, -v154
	v_fma_f32 v163, v163, s58, -v154
	v_fma_f32 v164, v164, s58, -v154
	v_fma_f32 v165, v165, s58, -v154
	v_max3_f32 v177, v161, v162, v163
	s_nop 0
	v_max3_f32 v178, v164, v165, v165
	s_nop 0
	v_max3_f32 v176, v176, v177, v178
	v_cndmask_b32_e32 v177, v226, v167, vcc
	v_cmp_gt_f32_e32 vcc, v176, v177
	s_cbranch_vccz .LBB0_673
	v_add_f32_e32 v176, v154, v176
	v_mov_b32_e32 v177, v176
	s_nop 1
	v_permlane16_swap_b32 v177, v176
	s_nop 0
	v_max_f32_e32 v176, v176, v176
	v_max_f32_e32 v177, v177, v177
	v_max_f32_e32 v176, v177, v176
	v_mov_b32_e32 v177, v176
	s_nop 1
	v_permlane32_swap_b32 v176, v177
	s_nop 0
	v_max3_f32 v177, v175, v176, v177
	v_cmp_neq_f32_e32 vcc, v177, v167
	s_nop 1
	v_cndmask_b32_e32 v178, 0, v177, vcc
	v_sub_f32_e32 v175, v175, v178
	v_exp_f32_e32 v176, v175
	v_sub_f32_e32 v154, v178, v154
	v_sub_f32_e32 v158, v158, v154
	v_sub_f32_e32 v159, v159, v154
	v_pk_mul_f32 v[98:99], v[98:99], v[176:177] op_sel_hi:[1,0]
	v_pk_mul_f32 v[96:97], v[96:97], v[176:177] op_sel_hi:[1,0]
	v_pk_mul_f32 v[94:95], v[94:95], v[176:177] op_sel_hi:[1,0]
	v_pk_mul_f32 v[92:93], v[92:93], v[176:177] op_sel_hi:[1,0]
	v_pk_mul_f32 v[90:91], v[90:91], v[176:177] op_sel_hi:[1,0]
	v_pk_mul_f32 v[88:89], v[88:89], v[176:177] op_sel_hi:[1,0]
	v_pk_mul_f32 v[78:79], v[78:79], v[176:177] op_sel_hi:[1,0]
	v_pk_mul_f32 v[76:77], v[76:77], v[176:177] op_sel_hi:[1,0]
	v_pk_mul_f32 v[74:75], v[74:75], v[176:177] op_sel_hi:[1,0]
	v_pk_mul_f32 v[72:73], v[72:73], v[176:177] op_sel_hi:[1,0]
	v_sub_f32_e32 v160, v160, v154
	v_sub_f32_e32 v161, v161, v154
	v_sub_f32_e32 v162, v162, v154
	v_sub_f32_e32 v163, v163, v154
	v_sub_f32_e32 v164, v164, v154
	v_sub_f32_e32 v165, v165, v154
	v_mov_b32_e32 v175, v177
	v_mov_b32_e32 v154, v178
.LBB0_673:
	v_mfma_f32_16x16x32_bf16 v[120:123], v[120:123], v[32:35], 0
	v_exp_f32_e32 v158, v158
	v_exp_f32_e32 v159, v159
	v_exp_f32_e32 v160, v160
	v_mfma_f32_16x16x32_bf16 v[116:119], v[116:119], v[32:35], 0
	v_exp_f32_e32 v161, v161
	v_exp_f32_e32 v162, v162
	v_exp_f32_e32 v163, v163
	v_exp_f32_e32 v164, v164
	v_exp_f32_e32 v165, v165
	v_lshrrev_b64 v[182:183], v144, v[156:157]
	v_bfe_i32 v156, v182, 0, 1
	v_bfe_i32 v157, v182, 1, 1
	v_bfe_i32 v176, v182, 2, 1
	v_bfe_i32 v177, v182, 3, 1
	v_bfe_i32 v178, v182, 4, 1
	v_bfe_i32 v179, v182, 5, 1
	v_bfe_i32 v180, v182, 6, 1
	v_bfe_i32 v181, v182, 7, 1
	v_mfma_f32_16x16x32_bf16 v[120:123], v[128:131], v[36:39], v[120:123]
	v_and_b32_e32 v183, 0xffff, v156
	v_and_b32_e32 v187, 0xffff0000, v157
	v_and_b32_e32 v188, 0xffff, v176
	v_mfma_f32_16x16x32_bf16 v[124:127], v[124:127], v[36:39], v[116:119]
	v_and_b32_e32 v189, 0xffff0000, v177
	v_and_b32_e32 v190, 0xffff, v178
	v_and_b32_e32 v191, 0xffff0000, v179
	v_and_b32_e32 v192, 0xffff, v180
	v_and_b32_e32 v182, 0xffff0000, v181
	v_cvt_pk_bf16_f32 v158, v158, v159
	v_cvt_pk_bf16_f32 v159, v160, v161
	v_cvt_pk_bf16_f32 v160, v162, v163
	v_cvt_pk_bf16_f32 v161, v164, v165
	v_bitop3_b32 v158, v187, v158, v183 bitop3:0xc8
	v_bitop3_b32 v159, v189, v159, v188 bitop3:0xc8
	v_bitop3_b32 v160, v191, v160, v190 bitop3:0xc8
	v_bitop3_b32 v161, v182, v161, v192 bitop3:0xc8
	v_fma_f32 v116, v120, s58, -v152
	v_fma_f32 v117, v121, s58, -v152
	v_fma_f32 v118, v122, s58, -v152
	v_fma_f32 v119, v123, s58, -v152
	v_mfma_f32_16x16x32_bf16 v[96:99], v[64:67], v[158:161], v[96:99]
	v_fma_f32 v120, v124, s58, -v152
	v_fma_f32 v121, v125, s58, -v152
	v_max3_f32 v124, v116, v117, v118
	v_cmp_eq_f32_e32 vcc, v174, v167
	s_waitcnt lgkmcnt(3)
	v_mfma_f32_16x16x32_bf16 v[92:95], v[104:107], v[158:161], v[92:95]
	v_max3_f32 v125, v119, v120, v121
	v_fma_f32 v122, v126, s58, -v152
	v_fma_f32 v123, v127, s58, -v152
	s_waitcnt lgkmcnt(2)
	v_mfma_f32_16x16x32_bf16 v[88:91], v[108:111], v[158:161], v[88:91]
	v_max3_f32 v126, v122, v123, v123
	s_nop 0
	v_max3_f32 v124, v124, v125, v126
	s_waitcnt lgkmcnt(1)
	v_mfma_f32_16x16x32_bf16 v[76:79], v[112:115], v[158:161], v[76:79]
	v_cndmask_b32_e32 v125, v226, v167, vcc
	v_cmp_gt_f32_e32 vcc, v124, v125
	s_waitcnt lgkmcnt(0)
	v_mfma_f32_16x16x32_bf16 v[72:75], v[100:103], v[158:161], v[72:75]
	s_cbranch_vccz .LBB0_675
	v_add_f32_e32 v124, v152, v124
	v_mov_b32_e32 v125, v124
	s_nop 1
	v_permlane16_swap_b32 v124, v125
	s_nop 0
	v_max_f32_e32 v125, v125, v125
	v_max_f32_e32 v124, v124, v124
	v_max_f32_e32 v124, v124, v125
	v_mov_b32_e32 v125, v124
	s_nop 1
	v_permlane32_swap_b32 v125, v124
	s_nop 0
	v_max3_f32 v125, v174, v125, v124
	v_cmp_neq_f32_e32 vcc, v125, v167
	s_nop 1
	v_cndmask_b32_e32 v126, 0, v125, vcc
	v_sub_f32_e32 v124, v174, v126
	v_exp_f32_e32 v124, v124
	v_sub_f32_e32 v127, v126, v152
	v_sub_f32_e32 v116, v116, v127
	v_sub_f32_e32 v117, v117, v127
	v_pk_mul_f32 v[70:71], v[70:71], v[124:125] op_sel_hi:[1,0]
	v_pk_mul_f32 v[68:69], v[68:69], v[124:125] op_sel_hi:[1,0]
	v_pk_mul_f32 v[62:63], v[62:63], v[124:125] op_sel_hi:[1,0]
	v_pk_mul_f32 v[60:61], v[60:61], v[124:125] op_sel_hi:[1,0]
	v_pk_mul_f32 v[58:59], v[58:59], v[124:125] op_sel_hi:[1,0]
	v_pk_mul_f32 v[56:57], v[56:57], v[124:125] op_sel_hi:[1,0]
	v_pk_mul_f32 v[6:7], v[6:7], v[124:125] op_sel_hi:[1,0]
	v_pk_mul_f32 v[4:5], v[4:5], v[124:125] op_sel_hi:[1,0]
	v_pk_mul_f32 v[2:3], v[2:3], v[124:125] op_sel_hi:[1,0]
	v_pk_mul_f32 v[0:1], v[0:1], v[124:125] op_sel_hi:[1,0]
	v_sub_f32_e32 v118, v118, v127
	v_sub_f32_e32 v119, v119, v127
	v_sub_f32_e32 v120, v120, v127
	v_sub_f32_e32 v121, v121, v127
	v_sub_f32_e32 v122, v122, v127
	v_sub_f32_e32 v123, v123, v127
	v_mov_b32_e32 v174, v125
	v_mov_b32_e32 v152, v126
